# v27 + router weight/bias kernarg pointers (0xb0, 0xb8) cached in v255 lanes 57-60; route_a prologue s_loads become v_readlane
# speedup vs baseline: 1.0069x; 1.0069x over previous
; #define LAS __attribute__((address_space(3)))
; #define KIN(i) (kargs()->in[i])
; #define KWS (kargs()->ws)
; #define REP(id) for (int rep_ = 0; rep_ < ((DUP_ID == (id)) ? DUP_N : 1); ++rep_)
; __global__ void __launch_bounds__(512, 2) mega(Ptrs Pdummy) {
;     extern __shared__ __attribute__((aligned(16))) unsigned char lds_raw[];
;     LAS unsigned char* lds = (LAS unsigned char*)lds_raw;
;     const int G = (int)gridDim.x, c = (int)blockIdx.x, wbase = __builtin_amdgcn_readfirstlane((int)threadIdx.x) & ~63;
;     { volatile LAS unsigned* MISC0 = (volatile LAS unsigned*)(lds + LDSCTL_OFF); if (threadIdx.x < 64) MISC0[threadIdx.x] = 0u; }
;     __syncthreads();
;     (void)xcd_barrier_post((unsigned*)(KWS + WS_CTL) + CW_BAR, (volatile LAS unsigned*)(lds + LDSCTL_OFF) + 8);
;     ...
;             REP(12) { unsigned char* ws = KWS; moe::route_a(lds, HBUF(hc), SBUF(sc), KIN(18) + l * DM, KIN(22) + (size_t)(l >> 1) * DM * NEXP, KIN(23) + (l >> 1) * NEXP, (int*)(ws + WS_SEL), (float*)(ws + WS_SEL + 256 * 1024), (int*)(ws + WS_SLOT + 964 * 1024), G, c, wbase); }
_Z4mega4Ptrs:
	s_mov_b64 s[88:89], s[0:1]
	s_load_dword s60, s[0:1], 0x100
	s_load_dwordx2 s[100:101], s[0:1], 0xf8
	s_load_dwordx4 s[4:7], s[0:1], 0xc0
	s_load_dwordx2 s[8:9], s[0:1], 0xd0
	s_load_dwordx2 s[10:11], s[0:1], 0x90
	s_load_dwordx4 s[12:15], s[0:1], 0xb0
	s_waitcnt lgkmcnt(0)
	v_writelane_b32 v255, s4, 49
	v_writelane_b32 v255, s5, 50
	v_writelane_b32 v255, s6, 51
	v_writelane_b32 v255, s7, 52
	v_writelane_b32 v255, s8, 53
	v_writelane_b32 v255, s9, 54
	v_writelane_b32 v255, s10, 55
	v_writelane_b32 v255, s11, 56
	v_writelane_b32 v255, s12, 57
	v_writelane_b32 v255, s13, 58
	v_writelane_b32 v255, s14, 59
	v_writelane_b32 v255, s15, 60
	s_add_u32 s0, s88, 0x100
	s_addc_u32 s1, s89, 0
	s_mov_b32 s92, s2
	v_writelane_b32 v255, s0, 0
	v_cmp_gt_u32_e32 vcc, 64, v0
	s_nop 0
	v_writelane_b32 v255, s1, 1
	v_readfirstlane_b32 s0, v0
	s_and_saveexec_b64 s[2:3], vcc
	v_lshl_add_u32 v1, v0, 2, 0
	v_add_u32_e32 v1, 0x20000, v1
	v_mov_b32_e32 v2, 0
	ds_write_b32 v1, v2
	s_or_b64 exec, exec, s[2:3]
	s_mov_b64 s[4:5], s[88:89]
	s_waitcnt lgkmcnt(0)
	s_barrier
	s_getreg_b32 s1, hwreg(HW_REG_XCC_ID, 0, 4)
	v_cmp_eq_u32_e32 vcc, 0, v0
	s_and_saveexec_b64 s[2:3], vcc
	s_cbranch_execz .LBB0_5
	s_mov_b64 s[6:7], exec
	v_mbcnt_lo_u32_b32 v0, s6, 0
	v_mbcnt_hi_u32_b32 v0, s7, v0
	v_cmp_eq_u32_e32 vcc, 0, v0
	s_and_b64 s[8:9], exec, vcc
	s_mov_b64 exec, s[8:9]
	s_cbranch_execz .LBB0_5
	s_mov_b64 s[4:5], s[100:101]
	s_lshl_b32 s1, s1, 8
	s_and_b32 s1, s1, 0xf00
	v_mov_b32_e32 v0, 0x4000
	s_waitcnt lgkmcnt(0)
	s_add_u32 s4, s4, s1
	s_addc_u32 s5, s5, 0
	s_bcnt1_i32_b64 s1, s[6:7]
	v_mov_b32_e32 v1, s1
	global_atomic_add v0, v1, s[4:5] offset:1024

; #define LAS __attribute__((address_space(3)))
; __device__ __forceinline__ int opaque_tid(int wbase) { int t = wbase + lane_id(); asm volatile("" : "+v"(t)); return t; }
; __device__ __forceinline__ int opaque_s(int x) { asm volatile("" : "+s"(x)); return x; }
; __device__ __forceinline__ void route_a(LAS unsigned char* lds, const bf16* h, const float* ssq, const float* gain, const float* rw, const float* rb, int* sel, float* selw, int* CNT, int G, int c, int wbase) {
;     const int tid = opaque_tid(wbase), lane = tid & 63, wid = __builtin_amdgcn_readfirstlane(tid >> 6); LAS int* lc = (LAS int*)lds; G = opaque_s(G); c = opaque_s(c);
;     f32x4 wg[4][4][2];
; #pragma unroll
;     for (int j = 0; j < 4; ++j) { const f32x4 gk = *(const f32x4*)(gain + 4 * lane + 256 * j);
; #pragma unroll
;         for (int q = 0; q < 4; ++q) { const float* wp = rw + (size_t)(4 * lane + 256 * j + q) * 8; wg[j][q][0] = *(const f32x4*)wp * gk[q]; wg[j][q][1] = *(const f32x4*)(wp + 4) * gk[q]; } }
;     float rbv[8];
; #pragma unroll
;     for (int e = 0; e < 8; ++e) rbv[e] = rb[e];
.LBB0_1104:
	s_or_b64 exec, exec, s[36:37]
	v_readlane_b32 s2, v255, 31
	v_readlane_b32 s3, v255, 32
	s_andn2_b64 vcc, exec, s[2:3]
	s_mov_b64 s[2:3], -1
	s_waitcnt lgkmcnt(0)
	s_barrier
	s_cbranch_vccnz .LBB0_1616
	s_mov_b64 s[8:9], s[88:89]
	s_mov_b64 s[4:5], s[88:89]
	s_mov_b64 s[6:7], s[88:89]
	s_mov_b64 s[2:3], s[88:89]
	s_mov_b32 s1, s38
	v_readlane_b32 s10, v255, 4
	v_mbcnt_lo_u32_b32 v0, s1, 0
	v_mbcnt_hi_u32_b32 v0, s1, v0
	v_add_u32_e32 v170, s93, v0
	s_mov_b32 s1, s10
	s_mov_b32 s33, s92
	s_cmpk_lt_i32 s33, 0x100
	v_readfirstlane_b32 s12, v170
	v_readlane_b32 s11, v255, 5
	s_cbranch_scc0 .LBB0_1118
	s_mov_b64 s[24:25], s[100:101]
	s_nop 0
	v_readlane_b32 s4, v255, 55
	v_readlane_b32 s5, v255, 56
	v_readlane_b32 s8, v255, 33
	s_lshr_b32 s13, s95, 1
	v_readlane_b32 s9, v255, 34
	v_readlane_b32 s6, v255, 57
	v_readlane_b32 s7, v255, 58
	s_lshl_b32 s10, s13, 13
	s_lshl_b32 s14, s13, 3
	s_lshl_b64 s[8:9], s[8:9], 2
	s_waitcnt lgkmcnt(0)
	s_add_u32 s4, s4, s8
	v_and_b32_e32 v8, 63, v170
	s_mov_b32 s11, s40
	s_addc_u32 s5, s5, s9
	v_lshlrev_b32_e32 v2, 4, v8
	s_lshl_b64 s[8:9], s[10:11], 2
	global_load_dwordx4 v[4:7], v2, s[4:5]
	s_add_u32 s6, s6, s8
	s_addc_u32 s7, s7, s9
	v_lshlrev_b32_e32 v232, 7, v8
	v_readlane_b32 s2, v255, 59
	v_readlane_b32 s3, v255, 60
	global_load_dwordx4 v[10:13], v232, s[6:7] offset:48
	global_load_dwordx4 v[24:27], v232, s[6:7] offset:32
	global_load_dwordx4 v[20:23], v232, s[6:7] offset:16
	global_load_dwordx4 v[16:19], v232, s[6:7]
	v_lshl_add_u64 v[0:1], s[6:7], 0, v[232:233]
	v_lshl_add_u64 v[14:15], v[0:1], 0, s[70:71]
	s_mov_b32 s15, s40
	s_lshl_b64 s[8:9], s[14:15], 2
	s_waitcnt lgkmcnt(0)
	s_add_u32 s2, s2, s8
	s_addc_u32 s3, s3, s9
	s_add_u32 s34, s24, 0x17600000
	s_addc_u32 s35, s25, 0
	s_add_u32 s36, s24, 0x17640000
	s_addc_u32 s37, s25, 0
	s_add_u32 s10, s24, 0x177f1000
	s_addc_u32 s11, s25, 0
	v_and_b32_e32 v9, 3, v170
	s_mov_b32 s41, 0
	v_lshl_add_u32 v171, v170, 2, 0
	s_waitcnt vmcnt(3)
	v_pk_mul_f32 v[28:29], v[4:5], v[10:11] op_sel:[1,0]
	v_pk_mul_f32 v[30:31], v[4:5], v[12:13] op_sel:[1,0]
	global_load_dwordx4 v[10:13], v232, s[6:7] offset:112
	global_load_dwordx4 v[40:43], v232, s[6:7] offset:96
	global_load_dwordx4 v[36:39], v232, s[6:7] offset:80
	global_load_dwordx4 v[32:35], v232, s[6:7] offset:64
	s_movk_i32 s6, 0x2000
	v_add_co_u32_e32 v64, vcc, s6, v0
	s_waitcnt vmcnt(4)
	v_pk_mul_f32 v[16:17], v[4:5], v[16:17] op_sel_hi:[0,1]
	v_pk_mul_f32 v[18:19], v[4:5], v[18:19] op_sel_hi:[0,1]
	v_pk_mul_f32 v[20:21], v[4:5], v[20:21] op_sel_hi:[0,1]
	v_pk_mul_f32 v[22:23], v[4:5], v[22:23] op_sel_hi:[0,1]
	v_pk_mul_f32 v[24:25], v[4:5], v[24:25] op_sel:[1,0]
	v_pk_mul_f32 v[26:27], v[4:5], v[26:27] op_sel:[1,0]
	v_mov_b32_e32 v4, v7
	v_addc_co_u32_e32 v65, vcc, 0, v1, vcc
	s_mov_b64 s[6:7], 0x2040
	s_waitcnt vmcnt(3)
	v_pk_mul_f32 v[44:45], v[4:5], v[10:11] op_sel_hi:[0,1]
	s_waitcnt vmcnt(2)
	v_pk_mul_f32 v[40:41], v[4:5], v[40:41] op_sel_hi:[0,1]
	s_waitcnt vmcnt(1)
	v_pk_mul_f32 v[36:37], v[6:7], v[36:37] op_sel_hi:[0,1]
	s_waitcnt vmcnt(0)
	v_pk_mul_f32 v[32:33], v[6:7], v[32:33] op_sel_hi:[0,1]
	v_pk_mul_f32 v[34:35], v[6:7], v[34:35] op_sel_hi:[0,1]
	v_pk_mul_f32 v[38:39], v[6:7], v[38:39] op_sel_hi:[0,1]
	v_pk_mul_f32 v[42:43], v[4:5], v[42:43] op_sel_hi:[0,1]
	v_pk_mul_f32 v[46:47], v[4:5], v[12:13] op_sel_hi:[0,1]
	global_load_dwordx4 v[4:7], v2, s[4:5] offset:1024
	global_load_dwordx4 v[10:13], v[64:65], off
	global_load_dwordx4 v[60:63], v[14:15], off offset:48
	global_load_dwordx4 v[56:59], v[14:15], off offset:32
	global_load_dwordx4 v[52:55], v[14:15], off offset:16
	s_waitcnt vmcnt(3)
	v_pk_mul_f32 v[48:49], v[4:5], v[12:13] op_sel_hi:[0,1]
	v_pk_mul_f32 v[50:51], v[4:5], v[10:11] op_sel_hi:[0,1]
	s_waitcnt vmcnt(0)
	v_pk_mul_f32 v[52:53], v[4:5], v[52:53] op_sel_hi:[0,1]
	v_pk_mul_f32 v[54:55], v[4:5], v[54:55] op_sel_hi:[0,1]
	v_pk_mul_f32 v[56:57], v[4:5], v[56:57] op_sel:[1,0]
	v_pk_mul_f32 v[58:59], v[4:5], v[58:59] op_sel:[1,0]
	v_pk_mul_f32 v[60:61], v[4:5], v[60:61] op_sel:[1,0]
	v_pk_mul_f32 v[62:63], v[4:5], v[62:63] op_sel:[1,0]
	v_lshl_add_u64 v[4:5], v[0:1], 0, s[6:7]
	global_load_dwordx4 v[10:13], v[64:65], off offset:64
	global_load_dwordx4 v[76:79], v[4:5], off offset:48
	global_load_dwordx4 v[72:75], v[4:5], off offset:32
	global_load_dwordx4 v[68:71], v[4:5], off offset:16
	s_mov_b64 s[6:7], 0x4000
	v_lshl_add_u64 v[14:15], v[0:1], 0, s[6:7]
	s_movk_i32 s6, 0x4000
	v_add_co_u32_e32 v96, vcc, s6, v0
	v_mov_b32_e32 v4, v7
	s_nop 0
	v_addc_co_u32_e32 v97, vcc, 0, v1, vcc
	s_mov_b64 s[6:7], 0x4040
	s_waitcnt vmcnt(3)
; __device__ __forceinline__ void route_a(LAS unsigned char* lds, const bf16* h, const float* ssq, const float* gain, const float* rw, const float* rb, int* sel, float* selw, int* CNT, int G, int c, int wbase) {
;     ...
;     f32x4 wg[4][4][2];
; #pragma unroll
;     for (int j = 0; j < 4; ++j) { const f32x4 gk = *(const f32x4*)(gain + 4 * lane + 256 * j);
; #pragma unroll
;         for (int q = 0; q < 4; ++q) { const float* wp = rw + (size_t)(4 * lane + 256 * j + q) * 8; wg[j][q][0] = *(const f32x4*)wp * gk[q]; wg[j][q][1] = *(const f32x4*)(wp + 4) * gk[q]; } }
;     float rbv[8];
; #pragma unroll
;     for (int e = 0; e < 8; ++e) rbv[e] = rb[e];
;     for (int chunk = c; chunk < NCHUNK; chunk += G) {
	v_pk_mul_f32 v[64:65], v[6:7], v[12:13] op_sel_hi:[0,1]
	v_pk_mul_f32 v[66:67], v[6:7], v[10:11] op_sel_hi:[0,1]
	s_waitcnt vmcnt(1)
	v_pk_mul_f32 v[72:73], v[4:5], v[72:73] op_sel_hi:[0,1]
	s_waitcnt vmcnt(0)
	v_pk_mul_f32 v[68:69], v[6:7], v[68:69] op_sel_hi:[0,1]
	v_pk_mul_f32 v[70:71], v[6:7], v[70:71] op_sel_hi:[0,1]
	v_pk_mul_f32 v[74:75], v[4:5], v[74:75] op_sel_hi:[0,1]
	v_pk_mul_f32 v[76:77], v[4:5], v[76:77] op_sel_hi:[0,1]
	v_pk_mul_f32 v[78:79], v[4:5], v[78:79] op_sel_hi:[0,1]
	global_load_dwordx4 v[4:7], v2, s[4:5] offset:2048
	global_load_dwordx4 v[10:13], v[96:97], off
	global_load_dwordx4 v[92:95], v[14:15], off offset:48
	global_load_dwordx4 v[88:91], v[14:15], off offset:32
	global_load_dwordx4 v[84:87], v[14:15], off offset:16
	s_waitcnt vmcnt(3)
	v_pk_mul_f32 v[80:81], v[4:5], v[12:13] op_sel_hi:[0,1]
	v_pk_mul_f32 v[82:83], v[4:5], v[10:11] op_sel_hi:[0,1]
	s_waitcnt vmcnt(0)
	v_pk_mul_f32 v[84:85], v[4:5], v[84:85] op_sel_hi:[0,1]
	v_pk_mul_f32 v[86:87], v[4:5], v[86:87] op_sel_hi:[0,1]
	v_pk_mul_f32 v[88:89], v[4:5], v[88:89] op_sel:[1,0]
	v_pk_mul_f32 v[90:91], v[4:5], v[90:91] op_sel:[1,0]
	v_pk_mul_f32 v[92:93], v[4:5], v[92:93] op_sel:[1,0]
	v_pk_mul_f32 v[94:95], v[4:5], v[94:95] op_sel:[1,0]
	v_lshl_add_u64 v[4:5], v[0:1], 0, s[6:7]
	global_load_dwordx4 v[10:13], v[96:97], off offset:64
	global_load_dwordx4 v[108:111], v[4:5], off offset:48
	global_load_dwordx4 v[104:107], v[4:5], off offset:32
	global_load_dwordx4 v[100:103], v[4:5], off offset:16
	v_mov_b32_e32 v4, v7
	s_waitcnt vmcnt(3)
	v_pk_mul_f32 v[96:97], v[6:7], v[12:13] op_sel_hi:[0,1]
	s_waitcnt vmcnt(2)
	v_pk_mul_f32 v[108:109], v[4:5], v[108:109] op_sel_hi:[0,1]
	s_waitcnt vmcnt(1)
	v_pk_mul_f32 v[104:105], v[4:5], v[104:105] op_sel_hi:[0,1]
	v_pk_mul_f32 v[106:107], v[4:5], v[106:107] op_sel_hi:[0,1]
	v_pk_mul_f32 v[110:111], v[4:5], v[110:111] op_sel_hi:[0,1]
	global_load_dwordx4 v[2:5], v2, s[4:5] offset:3072
	s_mov_b64 s[4:5], 0x6000
	v_pk_mul_f32 v[98:99], v[6:7], v[10:11] op_sel_hi:[0,1]
	s_waitcnt vmcnt(1)
	v_pk_mul_f32 v[100:101], v[6:7], v[100:101] op_sel_hi:[0,1]
	v_pk_mul_f32 v[102:103], v[6:7], v[102:103] op_sel_hi:[0,1]
	v_lshl_add_u64 v[6:7], v[0:1], 0, s[4:5]
	s_movk_i32 s4, 0x6000
	v_add_co_u32_e32 v14, vcc, s4, v0
	s_mov_b64 s[4:5], 0x6040
	s_nop 0
	v_addc_co_u32_e32 v15, vcc, 0, v1, vcc
	global_load_dwordx4 v[10:13], v[14:15], off
	global_load_dwordx4 v[124:127], v[6:7], off offset:48
	global_load_dwordx4 v[120:123], v[6:7], off offset:32
	global_load_dwordx4 v[116:119], v[6:7], off offset:16
	v_lshl_add_u64 v[6:7], v[0:1], 0, s[4:5]
	v_cmp_eq_u32_e64 s[4:5], 0, v8
	s_waitcnt vmcnt(3)
	v_pk_mul_f32 v[112:113], v[2:3], v[12:13] op_sel_hi:[0,1]
	v_pk_mul_f32 v[114:115], v[2:3], v[10:11] op_sel_hi:[0,1]
	s_waitcnt vmcnt(1)
	v_pk_mul_f32 v[120:121], v[2:3], v[120:121] op_sel:[1,0]
	s_waitcnt vmcnt(0)
	v_pk_mul_f32 v[116:117], v[2:3], v[116:117] op_sel_hi:[0,1]
	v_pk_mul_f32 v[118:119], v[2:3], v[118:119] op_sel_hi:[0,1]
	v_pk_mul_f32 v[122:123], v[2:3], v[122:123] op_sel:[1,0]
	v_pk_mul_f32 v[124:125], v[2:3], v[124:125] op_sel:[1,0]
	v_pk_mul_f32 v[126:127], v[2:3], v[126:127] op_sel:[1,0]
	global_load_dwordx4 v[0:3], v[14:15], off offset:64
	global_load_dwordx4 v[10:13], v[6:7], off offset:48
	global_load_dwordx4 v[136:139], v[6:7], off offset:32
	global_load_dwordx4 v[132:135], v[6:7], off offset:16
	s_waitcnt vmcnt(3)
	v_pk_mul_f32 v[130:131], v[4:5], v[0:1] op_sel_hi:[0,1]
	v_mov_b32_e32 v0, v5
	v_pk_mul_f32 v[128:129], v[4:5], v[2:3] op_sel_hi:[0,1]
	s_waitcnt vmcnt(0)
	v_pk_mul_f32 v[132:133], v[4:5], v[132:133] op_sel_hi:[0,1]
	v_pk_mul_f32 v[134:135], v[4:5], v[134:135] op_sel_hi:[0,1]
	v_pk_mul_f32 v[136:137], v[0:1], v[136:137] op_sel_hi:[0,1]
	v_pk_mul_f32 v[138:139], v[0:1], v[138:139] op_sel_hi:[0,1]
	v_pk_mul_f32 v[140:141], v[0:1], v[10:11] op_sel_hi:[0,1]
	v_pk_mul_f32 v[142:143], v[0:1], v[12:13] op_sel_hi:[0,1]
	global_load_dwordx4 v[0:3], v233, s[2:3]
	global_load_dwordx4 v[4:7], v233, s[2:3] offset:16
	v_readlane_b32 s2, v255, 10
	s_cmp_eq_u32 s2, 0
	s_mov_b32 s2, 0x13200000
	s_cselect_b32 s6, s2, 0x1b800000
	s_ashr_i32 s2, s12, 2
	s_and_b32 s7, s2, -16
	s_lshl_b32 s2, s2, 1
	s_lshl_b32 s42, s33, 8
	s_andn2_b32 s2, s2, 31
	s_add_i32 s42, s42, s2
	s_lshl_b32 s43, s1, 8
	v_readlane_b32 s2, v255, 11
	s_cmp_eq_u32 s2, 1
	s_cselect_b32 s8, 0, 0x200000
	v_lshl_or_b32 v232, v9, 4, s8
	s_mov_b64 s[8:9], 0x17200000
	v_lshl_add_u64 v[144:145], v[232:233], 0, s[8:9]
	s_lshl_b32 s8, s33, 7
	s_add_i32 s26, s8, s7
	v_cmp_gt_i32_e64 s[2:3], 8, v170
	s_or_b32 s28, s26, 1
	s_lshl_b32 s44, s1, 7
	v_lshl_or_b32 v232, v8, 3, s6
	s_branch .LBB0_1108
